# v59 plus P1 rotary epilogue: cos/sin loads of row groups 1-3 issued with group 0's and groups 5-6 with group 4's into spare VGPRs (8 serialized L2 round trips per rotary unit become about 3)
# speedup vs baseline: 1.0142x; 1.0142x over previous
.LBB0_122:
	v_cndmask_b32_e64 v166, v177, 1.0, s[28:29]
	v_lshl_add_u32 v168, s24, 8, v1
	s_andn2_b64 vcc, exec, s[30:31]
	v_mov_b32_e32 v167, v166
	s_cbranch_vccnz .LBB0_124
	v_ashrrev_i32_e32 v169, 31, v168
	v_lshlrev_b64 v[138:139], 9, v[168:169]
	v_lshl_add_u64 v[226:227], v[156:157], 0, v[138:139]
	v_lshl_add_u64 v[228:229], v[154:155], 0, v[138:139]
	s_mov_b32 s98, 0x2000
	s_mov_b32 s99, 0
	s_mov_b32 s100, 0xa000
	s_mov_b32 s101, 0
	v_lshl_add_u64 v[134:135], v[156:157], 0, v[138:139]
	global_load_dwordx4 v[130:133], v[134:135], off
	s_nop 0
	global_load_dwordx4 v[134:137], v[134:135], off offset:16
	v_lshl_add_u64 v[142:143], v[154:155], 0, v[138:139]
	global_load_dwordx4 v[138:141], v[142:143], off
	s_nop 0
	global_load_dwordx4 v[142:145], v[142:143], off offset:16
	v_lshl_add_u64 v[226:227], v[226:227], 0, s[98:99]
	v_lshl_add_u64 v[228:229], v[228:229], 0, s[98:99]
	global_load_dwordx4 v[186:189], v[226:227], off
	global_load_dwordx4 v[190:193], v[226:227], off offset:16
	global_load_dwordx4 v[194:197], v[228:229], off
	global_load_dwordx4 v[198:201], v[228:229], off offset:16
	v_lshl_add_u64 v[226:227], v[226:227], 0, s[98:99]
	v_lshl_add_u64 v[228:229], v[228:229], 0, s[98:99]
	global_load_dwordx4 v[202:205], v[226:227], off
	global_load_dwordx4 v[206:209], v[226:227], off offset:16
	global_load_dwordx4 v[210:213], v[228:229], off
	global_load_dwordx4 v[214:217], v[228:229], off offset:16
	v_lshl_add_u64 v[226:227], v[226:227], 0, s[98:99]
	v_lshl_add_u64 v[228:229], v[228:229], 0, s[98:99]
	global_load_dwordx4 v[236:239], v[226:227], off
	global_load_dwordx4 v[240:243], v[226:227], off offset:16
	global_load_dwordx4 v[244:247], v[228:229], off
	global_load_dwordx4 v[248:251], v[228:229], off offset:16
	v_mov_b32_e32 v170, v166
	v_mov_b32_e32 v171, v166
	s_waitcnt vmcnt(0)
	v_pk_mul_f32 v[178:179], v[120:121], v[132:133]
	v_pk_mul_f32 v[180:181], v[118:119], v[130:131]
	v_pk_mul_f32 v[182:183], v[116:117], v[136:137]
	v_pk_mul_f32 v[184:185], v[114:115], v[134:135]
	v_pk_mul_f32 v[132:133], v[128:129], v[132:133]
	v_pk_mul_f32 v[130:131], v[126:127], v[130:131]
	v_pk_mul_f32 v[136:137], v[124:125], v[136:137]
	v_pk_mul_f32 v[134:135], v[122:123], v[134:135]
	v_pk_fma_f32 v[128:129], v[128:129], v[140:141], v[178:179] neg_lo:[0,0,1] neg_hi:[0,0,1]
	v_pk_fma_f32 v[126:127], v[126:127], v[138:139], v[180:181] neg_lo:[0,0,1] neg_hi:[0,0,1]
	v_pk_fma_f32 v[124:125], v[124:125], v[144:145], v[182:183] neg_lo:[0,0,1] neg_hi:[0,0,1]
	v_pk_fma_f32 v[122:123], v[122:123], v[142:143], v[184:185] neg_lo:[0,0,1] neg_hi:[0,0,1]
	v_pk_fma_f32 v[120:121], v[120:121], v[140:141], v[132:133]
	v_pk_fma_f32 v[118:119], v[118:119], v[138:139], v[130:131]
	v_pk_fma_f32 v[116:117], v[116:117], v[144:145], v[136:137]
	v_pk_fma_f32 v[114:115], v[114:115], v[142:143], v[134:135]
	v_pk_mul_f32 v[132:133], v[170:171], v[128:129]
	v_pk_mul_f32 v[130:131], v[166:167], v[126:127]
	v_pk_mul_f32 v[136:137], v[170:171], v[124:125]
	v_pk_mul_f32 v[134:135], v[166:167], v[122:123]
	v_pk_mul_f32 v[140:141], v[170:171], v[120:121]
	v_pk_mul_f32 v[138:139], v[166:167], v[118:119]
	v_pk_mul_f32 v[144:145], v[170:171], v[116:117]
	v_pk_mul_f32 v[142:143], v[166:167], v[114:115]

.LBB0_132:
	s_andn2_b64 vcc, exec, s[24:25]
	v_or_b32_e32 v130, 16, v168
	s_cbranch_vccnz .LBB0_134
	v_ashrrev_i32_e32 v131, 31, v130
	v_lshlrev_b64 v[122:123], 9, v[130:131]
	v_lshl_add_u64 v[118:119], v[156:157], 0, v[122:123]
	v_mov_b64_e32 v[114:115], v[186:187]
	v_mov_b64_e32 v[116:117], v[188:189]
	s_nop 0
	v_mov_b64_e32 v[118:119], v[190:191]
	v_mov_b64_e32 v[120:121], v[192:193]
	v_lshl_add_u64 v[126:127], v[154:155], 0, v[122:123]
	v_mov_b64_e32 v[122:123], v[194:195]
	v_mov_b64_e32 v[124:125], v[196:197]
	s_nop 0
	v_mov_b64_e32 v[126:127], v[198:199]
	v_mov_b64_e32 v[128:129], v[200:201]
	v_mov_b32_e32 v132, v166
	v_mov_b32_e32 v133, v166
	v_pk_mul_f32 v[134:135], v[104:105], v[116:117]
	v_pk_mul_f32 v[136:137], v[102:103], v[114:115]
	v_pk_mul_f32 v[138:139], v[100:101], v[120:121]
	v_pk_mul_f32 v[140:141], v[98:99], v[118:119]
	v_pk_mul_f32 v[116:117], v[112:113], v[116:117]
	v_pk_mul_f32 v[114:115], v[110:111], v[114:115]
	v_pk_mul_f32 v[120:121], v[108:109], v[120:121]
	v_pk_mul_f32 v[118:119], v[106:107], v[118:119]
	v_pk_fma_f32 v[112:113], v[112:113], v[124:125], v[134:135] neg_lo:[0,0,1] neg_hi:[0,0,1]
	v_pk_fma_f32 v[110:111], v[110:111], v[122:123], v[136:137] neg_lo:[0,0,1] neg_hi:[0,0,1]
	v_pk_fma_f32 v[108:109], v[108:109], v[128:129], v[138:139] neg_lo:[0,0,1] neg_hi:[0,0,1]
	v_pk_fma_f32 v[106:107], v[106:107], v[126:127], v[140:141] neg_lo:[0,0,1] neg_hi:[0,0,1]
	v_pk_fma_f32 v[104:105], v[104:105], v[124:125], v[116:117]
	v_pk_fma_f32 v[102:103], v[102:103], v[122:123], v[114:115]
	v_pk_fma_f32 v[100:101], v[100:101], v[128:129], v[120:121]
	v_pk_fma_f32 v[98:99], v[98:99], v[126:127], v[118:119]
	v_pk_mul_f32 v[116:117], v[132:133], v[112:113]
	v_pk_mul_f32 v[114:115], v[166:167], v[110:111]
	v_pk_mul_f32 v[120:121], v[132:133], v[108:109]
	v_pk_mul_f32 v[118:119], v[166:167], v[106:107]
	v_pk_mul_f32 v[124:125], v[132:133], v[104:105]
	v_pk_mul_f32 v[122:123], v[166:167], v[102:103]
	v_pk_mul_f32 v[128:129], v[132:133], v[100:101]
	v_pk_mul_f32 v[126:127], v[166:167], v[98:99]

.LBB0_142:
	s_andn2_b64 vcc, exec, s[24:25]
	v_or_b32_e32 v114, 32, v168
	s_cbranch_vccnz .LBB0_144
	v_ashrrev_i32_e32 v115, 31, v114
	v_lshlrev_b64 v[106:107], 9, v[114:115]
	v_lshl_add_u64 v[102:103], v[156:157], 0, v[106:107]
	v_mov_b64_e32 v[98:99], v[202:203]
	v_mov_b64_e32 v[100:101], v[204:205]
	s_nop 0
	v_mov_b64_e32 v[102:103], v[206:207]
	v_mov_b64_e32 v[104:105], v[208:209]
	v_lshl_add_u64 v[110:111], v[154:155], 0, v[106:107]
	v_mov_b64_e32 v[106:107], v[210:211]
	v_mov_b64_e32 v[108:109], v[212:213]
	s_nop 0
	v_mov_b64_e32 v[110:111], v[214:215]
	v_mov_b64_e32 v[112:113], v[216:217]
	v_mov_b32_e32 v116, v166
	v_mov_b32_e32 v117, v166
	v_pk_mul_f32 v[118:119], v[88:89], v[100:101]
	v_pk_mul_f32 v[120:121], v[86:87], v[98:99]
	v_pk_mul_f32 v[122:123], v[84:85], v[104:105]
	v_pk_mul_f32 v[124:125], v[82:83], v[102:103]
	v_pk_mul_f32 v[100:101], v[96:97], v[100:101]
	v_pk_mul_f32 v[98:99], v[94:95], v[98:99]
	v_pk_mul_f32 v[104:105], v[92:93], v[104:105]
	v_pk_mul_f32 v[102:103], v[90:91], v[102:103]
	v_pk_fma_f32 v[96:97], v[96:97], v[108:109], v[118:119] neg_lo:[0,0,1] neg_hi:[0,0,1]
	v_pk_fma_f32 v[94:95], v[94:95], v[106:107], v[120:121] neg_lo:[0,0,1] neg_hi:[0,0,1]
	v_pk_fma_f32 v[92:93], v[92:93], v[112:113], v[122:123] neg_lo:[0,0,1] neg_hi:[0,0,1]
	v_pk_fma_f32 v[90:91], v[90:91], v[110:111], v[124:125] neg_lo:[0,0,1] neg_hi:[0,0,1]
	v_pk_fma_f32 v[88:89], v[88:89], v[108:109], v[100:101]
	v_pk_fma_f32 v[86:87], v[86:87], v[106:107], v[98:99]
	v_pk_fma_f32 v[84:85], v[84:85], v[112:113], v[104:105]
	v_pk_fma_f32 v[82:83], v[82:83], v[110:111], v[102:103]
	v_pk_mul_f32 v[100:101], v[116:117], v[96:97]
	v_pk_mul_f32 v[98:99], v[166:167], v[94:95]
	v_pk_mul_f32 v[104:105], v[116:117], v[92:93]
	v_pk_mul_f32 v[102:103], v[166:167], v[90:91]
	v_pk_mul_f32 v[108:109], v[116:117], v[88:89]
	v_pk_mul_f32 v[106:107], v[166:167], v[86:87]
	v_pk_mul_f32 v[112:113], v[116:117], v[84:85]
	v_pk_mul_f32 v[110:111], v[166:167], v[82:83]

.LBB0_152:
	s_andn2_b64 vcc, exec, s[24:25]
	v_or_b32_e32 v98, 48, v168
	s_cbranch_vccnz .LBB0_154
	v_ashrrev_i32_e32 v99, 31, v98
	v_lshlrev_b64 v[90:91], 9, v[98:99]
	v_lshl_add_u64 v[86:87], v[156:157], 0, v[90:91]
	v_mov_b64_e32 v[82:83], v[236:237]
	v_mov_b64_e32 v[84:85], v[238:239]
	s_nop 0
	v_mov_b64_e32 v[86:87], v[240:241]
	v_mov_b64_e32 v[88:89], v[242:243]
	v_lshl_add_u64 v[94:95], v[154:155], 0, v[90:91]
	v_mov_b64_e32 v[90:91], v[244:245]
	v_mov_b64_e32 v[92:93], v[246:247]
	s_nop 0
	v_mov_b64_e32 v[94:95], v[248:249]
	v_mov_b64_e32 v[96:97], v[250:251]
	v_lshl_add_u64 v[226:227], v[226:227], 0, s[100:101]
	v_lshl_add_u64 v[228:229], v[228:229], 0, s[100:101]
	global_load_dwordx4 v[186:189], v[226:227], off
	global_load_dwordx4 v[190:193], v[226:227], off offset:16
	global_load_dwordx4 v[194:197], v[228:229], off
	global_load_dwordx4 v[198:201], v[228:229], off offset:16
	v_lshl_add_u64 v[226:227], v[226:227], 0, s[98:99]
	v_lshl_add_u64 v[228:229], v[228:229], 0, s[98:99]
	global_load_dwordx4 v[202:205], v[226:227], off
	global_load_dwordx4 v[206:209], v[226:227], off offset:16
	global_load_dwordx4 v[210:213], v[228:229], off
	global_load_dwordx4 v[214:217], v[228:229], off offset:16
	v_lshl_add_u64 v[226:227], v[226:227], 0, s[98:99]
	v_lshl_add_u64 v[228:229], v[228:229], 0, s[98:99]
	global_load_dwordx4 v[236:239], v[226:227], off
	global_load_dwordx4 v[240:243], v[226:227], off offset:16
	global_load_dwordx4 v[244:247], v[228:229], off
	global_load_dwordx4 v[248:251], v[228:229], off offset:16
	v_mov_b32_e32 v100, v166
	v_mov_b32_e32 v101, v166
	v_pk_mul_f32 v[102:103], v[72:73], v[84:85]
	v_pk_mul_f32 v[104:105], v[70:71], v[82:83]
	v_pk_mul_f32 v[106:107], v[68:69], v[88:89]
	v_pk_mul_f32 v[108:109], v[66:67], v[86:87]
	v_pk_mul_f32 v[84:85], v[80:81], v[84:85]
	v_pk_mul_f32 v[82:83], v[78:79], v[82:83]
	v_pk_mul_f32 v[88:89], v[76:77], v[88:89]
	v_pk_mul_f32 v[86:87], v[74:75], v[86:87]
	v_pk_fma_f32 v[80:81], v[80:81], v[92:93], v[102:103] neg_lo:[0,0,1] neg_hi:[0,0,1]
	v_pk_fma_f32 v[78:79], v[78:79], v[90:91], v[104:105] neg_lo:[0,0,1] neg_hi:[0,0,1]
	v_pk_fma_f32 v[76:77], v[76:77], v[96:97], v[106:107] neg_lo:[0,0,1] neg_hi:[0,0,1]
	v_pk_fma_f32 v[74:75], v[74:75], v[94:95], v[108:109] neg_lo:[0,0,1] neg_hi:[0,0,1]
	v_pk_fma_f32 v[72:73], v[72:73], v[92:93], v[84:85]
	v_pk_fma_f32 v[70:71], v[70:71], v[90:91], v[82:83]
	v_pk_fma_f32 v[68:69], v[68:69], v[96:97], v[88:89]
	v_pk_fma_f32 v[66:67], v[66:67], v[94:95], v[86:87]
	v_pk_mul_f32 v[84:85], v[100:101], v[80:81]
	v_pk_mul_f32 v[82:83], v[166:167], v[78:79]
	v_pk_mul_f32 v[88:89], v[100:101], v[76:77]
	v_pk_mul_f32 v[86:87], v[166:167], v[74:75]
	v_pk_mul_f32 v[92:93], v[100:101], v[72:73]
	v_pk_mul_f32 v[90:91], v[166:167], v[70:71]
	v_pk_mul_f32 v[96:97], v[100:101], v[68:69]
	v_pk_mul_f32 v[94:95], v[166:167], v[66:67]

.LBB0_162:
	s_andn2_b64 vcc, exec, s[24:25]
	v_add_u32_e32 v82, 0x80, v168
	s_cbranch_vccnz .LBB0_164
	v_ashrrev_i32_e32 v83, 31, v82
	v_lshlrev_b64 v[74:75], 9, v[82:83]
	v_lshl_add_u64 v[70:71], v[156:157], 0, v[74:75]
	s_waitcnt vmcnt(0)
	v_mov_b64_e32 v[66:67], v[186:187]
	v_mov_b64_e32 v[68:69], v[188:189]
	s_nop 0
	v_mov_b64_e32 v[70:71], v[190:191]
	v_mov_b64_e32 v[72:73], v[192:193]
	v_lshl_add_u64 v[78:79], v[154:155], 0, v[74:75]
	v_mov_b64_e32 v[74:75], v[194:195]
	v_mov_b64_e32 v[76:77], v[196:197]
	s_nop 0
	v_mov_b64_e32 v[78:79], v[198:199]
	v_mov_b64_e32 v[80:81], v[200:201]
	v_mov_b32_e32 v84, v166
	v_mov_b32_e32 v85, v166
	v_pk_mul_f32 v[86:87], v[56:57], v[68:69]
	v_pk_mul_f32 v[88:89], v[54:55], v[66:67]
	v_pk_mul_f32 v[90:91], v[52:53], v[72:73]
	v_pk_mul_f32 v[92:93], v[50:51], v[70:71]
	v_pk_mul_f32 v[68:69], v[64:65], v[68:69]
	v_pk_mul_f32 v[66:67], v[62:63], v[66:67]
	v_pk_mul_f32 v[72:73], v[60:61], v[72:73]
	v_pk_mul_f32 v[70:71], v[58:59], v[70:71]
	v_pk_fma_f32 v[64:65], v[64:65], v[76:77], v[86:87] neg_lo:[0,0,1] neg_hi:[0,0,1]
	v_pk_fma_f32 v[62:63], v[62:63], v[74:75], v[88:89] neg_lo:[0,0,1] neg_hi:[0,0,1]
	v_pk_fma_f32 v[60:61], v[60:61], v[80:81], v[90:91] neg_lo:[0,0,1] neg_hi:[0,0,1]
	v_pk_fma_f32 v[58:59], v[58:59], v[78:79], v[92:93] neg_lo:[0,0,1] neg_hi:[0,0,1]
	v_pk_fma_f32 v[56:57], v[56:57], v[76:77], v[68:69]
	v_pk_fma_f32 v[54:55], v[54:55], v[74:75], v[66:67]
	v_pk_fma_f32 v[52:53], v[52:53], v[80:81], v[72:73]
	v_pk_fma_f32 v[50:51], v[50:51], v[78:79], v[70:71]
	v_pk_mul_f32 v[68:69], v[84:85], v[64:65]
	v_pk_mul_f32 v[66:67], v[166:167], v[62:63]
	v_pk_mul_f32 v[72:73], v[84:85], v[60:61]
	v_pk_mul_f32 v[70:71], v[166:167], v[58:59]
	v_pk_mul_f32 v[76:77], v[84:85], v[56:57]
	v_pk_mul_f32 v[74:75], v[166:167], v[54:55]
	v_pk_mul_f32 v[80:81], v[84:85], v[52:53]
	v_pk_mul_f32 v[78:79], v[166:167], v[50:51]

.LBB0_172:
	s_andn2_b64 vcc, exec, s[24:25]
	v_add_u32_e32 v66, 0x90, v168
	s_cbranch_vccnz .LBB0_174
	v_ashrrev_i32_e32 v67, 31, v66
	v_lshlrev_b64 v[58:59], 9, v[66:67]
	v_lshl_add_u64 v[54:55], v[156:157], 0, v[58:59]
	v_mov_b64_e32 v[50:51], v[202:203]
	v_mov_b64_e32 v[52:53], v[204:205]
	s_nop 0
	v_mov_b64_e32 v[54:55], v[206:207]
	v_mov_b64_e32 v[56:57], v[208:209]
	v_lshl_add_u64 v[62:63], v[154:155], 0, v[58:59]
	v_mov_b64_e32 v[58:59], v[210:211]
	v_mov_b64_e32 v[60:61], v[212:213]
	s_nop 0
	v_mov_b64_e32 v[62:63], v[214:215]
	v_mov_b64_e32 v[64:65], v[216:217]
	v_mov_b32_e32 v68, v166
	v_mov_b32_e32 v69, v166
	v_pk_mul_f32 v[70:71], v[40:41], v[52:53]
	v_pk_mul_f32 v[72:73], v[38:39], v[50:51]
	v_pk_mul_f32 v[74:75], v[36:37], v[56:57]
	v_pk_mul_f32 v[76:77], v[34:35], v[54:55]
	v_pk_mul_f32 v[52:53], v[48:49], v[52:53]
	v_pk_mul_f32 v[50:51], v[46:47], v[50:51]
	v_pk_mul_f32 v[56:57], v[44:45], v[56:57]
	v_pk_mul_f32 v[54:55], v[42:43], v[54:55]
	v_pk_fma_f32 v[48:49], v[48:49], v[60:61], v[70:71] neg_lo:[0,0,1] neg_hi:[0,0,1]
	v_pk_fma_f32 v[46:47], v[46:47], v[58:59], v[72:73] neg_lo:[0,0,1] neg_hi:[0,0,1]
	v_pk_fma_f32 v[44:45], v[44:45], v[64:65], v[74:75] neg_lo:[0,0,1] neg_hi:[0,0,1]
	v_pk_fma_f32 v[42:43], v[42:43], v[62:63], v[76:77] neg_lo:[0,0,1] neg_hi:[0,0,1]
	v_pk_fma_f32 v[40:41], v[40:41], v[60:61], v[52:53]
	v_pk_fma_f32 v[38:39], v[38:39], v[58:59], v[50:51]
	v_pk_fma_f32 v[36:37], v[36:37], v[64:65], v[56:57]
	v_pk_fma_f32 v[34:35], v[34:35], v[62:63], v[54:55]
	v_pk_mul_f32 v[52:53], v[68:69], v[48:49]
	v_pk_mul_f32 v[50:51], v[166:167], v[46:47]
	v_pk_mul_f32 v[56:57], v[68:69], v[44:45]
	v_pk_mul_f32 v[54:55], v[166:167], v[42:43]
	v_pk_mul_f32 v[60:61], v[68:69], v[40:41]
	v_pk_mul_f32 v[58:59], v[166:167], v[38:39]
	v_pk_mul_f32 v[64:65], v[68:69], v[36:37]
	v_pk_mul_f32 v[62:63], v[166:167], v[34:35]

.LBB0_182:
	s_andn2_b64 vcc, exec, s[24:25]
	v_add_u32_e32 v50, 0xa0, v168
	s_cbranch_vccnz .LBB0_184
	v_ashrrev_i32_e32 v51, 31, v50
	v_lshlrev_b64 v[42:43], 9, v[50:51]
	v_lshl_add_u64 v[38:39], v[156:157], 0, v[42:43]
	v_mov_b64_e32 v[34:35], v[236:237]
	v_mov_b64_e32 v[36:37], v[238:239]
	s_nop 0
	v_mov_b64_e32 v[38:39], v[240:241]
	v_mov_b64_e32 v[40:41], v[242:243]
	v_lshl_add_u64 v[46:47], v[154:155], 0, v[42:43]
	v_mov_b64_e32 v[42:43], v[244:245]
	v_mov_b64_e32 v[44:45], v[246:247]
	s_nop 0
	v_mov_b64_e32 v[46:47], v[248:249]
	v_mov_b64_e32 v[48:49], v[250:251]
	v_mov_b32_e32 v52, v166
	v_mov_b32_e32 v53, v166
	v_pk_mul_f32 v[54:55], v[24:25], v[36:37]
	v_pk_mul_f32 v[56:57], v[22:23], v[34:35]
	v_pk_mul_f32 v[58:59], v[20:21], v[40:41]
	v_pk_mul_f32 v[60:61], v[18:19], v[38:39]
	v_pk_mul_f32 v[36:37], v[32:33], v[36:37]
	v_pk_mul_f32 v[34:35], v[30:31], v[34:35]
	v_pk_mul_f32 v[40:41], v[28:29], v[40:41]
	v_pk_mul_f32 v[38:39], v[26:27], v[38:39]
	v_pk_fma_f32 v[32:33], v[32:33], v[44:45], v[54:55] neg_lo:[0,0,1] neg_hi:[0,0,1]
	v_pk_fma_f32 v[30:31], v[30:31], v[42:43], v[56:57] neg_lo:[0,0,1] neg_hi:[0,0,1]
	v_pk_fma_f32 v[28:29], v[28:29], v[48:49], v[58:59] neg_lo:[0,0,1] neg_hi:[0,0,1]
	v_pk_fma_f32 v[26:27], v[26:27], v[46:47], v[60:61] neg_lo:[0,0,1] neg_hi:[0,0,1]
	v_pk_fma_f32 v[24:25], v[24:25], v[44:45], v[36:37]
	v_pk_fma_f32 v[22:23], v[22:23], v[42:43], v[34:35]
	v_pk_fma_f32 v[20:21], v[20:21], v[48:49], v[40:41]
	v_pk_fma_f32 v[18:19], v[18:19], v[46:47], v[38:39]
	v_pk_mul_f32 v[36:37], v[52:53], v[32:33]
	v_pk_mul_f32 v[34:35], v[166:167], v[30:31]
	v_pk_mul_f32 v[40:41], v[52:53], v[28:29]
	v_pk_mul_f32 v[38:39], v[166:167], v[26:27]
	v_pk_mul_f32 v[44:45], v[52:53], v[24:25]
	v_pk_mul_f32 v[42:43], v[166:167], v[22:23]
	v_pk_mul_f32 v[48:49], v[52:53], v[20:21]
	v_pk_mul_f32 v[46:47], v[166:167], v[18:19]
